# V phase: packed-word loads use SGPR-pair bases (saddr form) - 7 address VALU per trip become SALU
# speedup vs baseline: 1.0062x; 1.0035x over previous
.LBB0_956:
	s_and_b32 s8, s3, 0x78
	s_add_i32 s8, s8, s4
	s_ashr_i32 s9, s8, 31
	s_lshl_b64 s[10:11], s[8:9], 15
	s_add_u32 s10, s12, s10
	s_addc_u32 s11, s13, s11
	s_and_b32 s17, s16, 0x1000
	s_lshl_b32 s17, s17, 2
	s_add_u32 s10, s10, s17
	s_addc_u32 s11, s11, 0
	s_add_u32 s62, s10, s6
	s_addc_u32 s63, s11, s7
	s_add_u32 s64, s10, s14
	s_addc_u32 s65, s11, 0
	s_mov_b32 s17, s18
	s_nop 0
	global_load_dword v104, v2, s[62:63] offset:256
	global_load_dword v106, v2, s[62:63] offset:512
	global_load_dword v108, v2, s[62:63] offset:768
	global_load_dword v110, v2, s[62:63] offset:1024
	global_load_dword v112, v2, s[62:63] offset:1280
	global_load_dword v114, v2, s[62:63] offset:1536
	global_load_dword v98, v2, s[62:63] offset:1792
	global_load_dword v100, v2, s[62:63] offset:2048
	global_load_dword v116, v2, s[64:65] offset:-4096
	global_load_dword v102, v2, s[62:63] offset:2304
	global_load_dword v78, v2, s[62:63] offset:2560
	global_load_dword v80, v2, s[62:63] offset:2816
	global_load_dword v82, v2, s[62:63] offset:3072
	global_load_dword v84, v2, s[62:63] offset:3328
	global_load_dword v86, v2, s[62:63] offset:3584
	global_load_dword v88, v2, s[62:63] offset:3840
	global_load_dword v90, v2, s[64:65]
	global_load_dword v92, v2, s[64:65] offset:256
	global_load_dword v94, v2, s[64:65] offset:512
	global_load_dword v96, v2, s[64:65] offset:768
	global_load_dword v76, v2, s[64:65] offset:1024
	global_load_dword v77, v2, s[64:65] offset:1280
	global_load_dword v56, v2, s[64:65] offset:1536
	global_load_dword v57, v2, s[64:65] offset:1792
	global_load_dword v58, v2, s[64:65] offset:2048
	global_load_dword v59, v2, s[64:65] offset:2304
	global_load_dword v60, v2, s[64:65] offset:2560
	global_load_dword v61, v2, s[64:65] offset:2816
	global_load_dword v62, v2, s[64:65] offset:3072
	global_load_dword v63, v2, s[64:65] offset:3328
	global_load_dword v54, v2, s[64:65] offset:3584
	global_load_dword v55, v2, s[64:65] offset:3840
	s_waitcnt vmcnt(56)
	v_and_b32_e32 v9, 0x1fff8, v64
	v_and_b32_e32 v11, 0x1fff8, v66
	v_and_b32_e32 v13, 0x1fff8, v68
	v_and_b32_e32 v15, 0x1fff8, v70
	ds_read_b64 v[126:127], v9
	ds_read_b64 v[128:129], v11
	ds_read_b64 v[130:131], v13
	ds_read_b64 v[132:133], v15
	v_and_b32_e32 v9, 0x1fff8, v72
	v_and_b32_e32 v11, 0x1fff8, v74
	v_and_b32_e32 v13, 0x1fff8, v48
	v_and_b32_e32 v15, 0x1fff8, v50
	ds_read_b64 v[134:135], v9
	ds_read_b64 v[136:137], v11
	ds_read_b64 v[138:139], v13
	ds_read_b64 v[140:141], v15
	s_setprio 1
	s_waitcnt lgkmcnt(7)
	v_cvt_pk_f32_fp8_e32 v[142:143], v126
	v_cvt_pk_f32_fp8_sdwa v[144:145], v126 src0_sel:WORD_1
	v_cvt_pk_f32_fp8_e32 v[146:147], v127
	v_cvt_pk_f32_fp8_sdwa v[126:127], v127 src0_sel:WORD_1
	s_waitcnt lgkmcnt(6)
	v_cvt_pk_f32_fp8_e32 v[148:149], v128
	v_cvt_pk_f32_fp8_sdwa v[150:151], v128 src0_sel:WORD_1
	v_cvt_pk_f32_fp8_e32 v[152:153], v129
	v_cvt_pk_f32_fp8_sdwa v[128:129], v129 src0_sel:WORD_1
	s_waitcnt lgkmcnt(5)
	v_cvt_pk_f32_fp8_e32 v[154:155], v130
	v_cvt_pk_f32_fp8_sdwa v[156:157], v130 src0_sel:WORD_1
	v_cvt_pk_f32_fp8_e32 v[158:159], v131
	v_cvt_pk_f32_fp8_sdwa v[130:131], v131 src0_sel:WORD_1
	s_waitcnt lgkmcnt(4)
	v_cvt_pk_f32_fp8_e32 v[160:161], v132
	v_cvt_pk_f32_fp8_sdwa v[162:163], v132 src0_sel:WORD_1
	v_cvt_pk_f32_fp8_e32 v[164:165], v133
	v_cvt_pk_f32_fp8_sdwa v[132:133], v133 src0_sel:WORD_1
	s_waitcnt lgkmcnt(3)
	v_cvt_pk_f32_fp8_e32 v[166:167], v134
	v_cvt_pk_f32_fp8_sdwa v[168:169], v134 src0_sel:WORD_1
	v_cvt_pk_f32_fp8_e32 v[170:171], v135
	v_cvt_pk_f32_fp8_sdwa v[134:135], v135 src0_sel:WORD_1
	s_waitcnt lgkmcnt(2)
	v_cvt_pk_f32_fp8_e32 v[172:173], v136
	v_cvt_pk_f32_fp8_sdwa v[174:175], v136 src0_sel:WORD_1
	v_cvt_pk_f32_fp8_e32 v[176:177], v137
	v_cvt_pk_f32_fp8_sdwa v[136:137], v137 src0_sel:WORD_1
	s_waitcnt lgkmcnt(1)
	v_cvt_pk_f32_fp8_e32 v[178:179], v138
	v_cvt_pk_f32_fp8_sdwa v[180:181], v138 src0_sel:WORD_1
	v_cvt_pk_f32_fp8_e32 v[182:183], v139
	v_cvt_pk_f32_fp8_sdwa v[138:139], v139 src0_sel:WORD_1
	s_waitcnt lgkmcnt(0)
	v_cvt_pk_f32_fp8_e32 v[184:185], v140
	v_cvt_pk_f32_fp8_sdwa v[186:187], v140 src0_sel:WORD_1
	v_cvt_pk_f32_fp8_e32 v[188:189], v141
	v_cvt_pk_f32_fp8_sdwa v[140:141], v141 src0_sel:WORD_1
	s_setprio 0
	s_waitcnt vmcnt(48)
	v_and_b32_e32 v9, 0x1fff8, v52
	v_and_b32_e32 v11, 0x1fff8, v32
	v_and_b32_e32 v13, 0x1fff8, v34
	v_and_b32_e32 v15, 0x1fff8, v36
	ds_read_b64 v[190:191], v9
	ds_read_b64 v[192:193], v11
	ds_read_b64 v[194:195], v13
	ds_read_b64 v[196:197], v15
	v_and_b32_e32 v9, 0x1fff8, v38
	v_and_b32_e32 v11, 0x1fff8, v40
	v_and_b32_e32 v13, 0x1fff8, v42
	v_and_b32_e32 v15, 0x1fff8, v44
	ds_read_b64 v[198:199], v9
	ds_read_b64 v[200:201], v11
	ds_read_b64 v[202:203], v13
	ds_read_b64 v[204:205], v15
	s_setprio 1
	v_pk_fma_f32 v[118:119], v[142:143], v[64:65], v[118:119] op_sel_hi:[1,0,1]
	v_pk_fma_f32 v[122:123], v[144:145], v[64:65], v[122:123] op_sel_hi:[1,0,1]
	v_pk_fma_f32 v[120:121], v[146:147], v[64:65], v[120:121] op_sel_hi:[1,0,1]
	v_pk_fma_f32 v[64:65], v[126:127], v[64:65], v[124:125] op_sel_hi:[1,0,1]
	v_pk_fma_f32 v[118:119], v[148:149], v[66:67], v[118:119] op_sel_hi:[1,0,1]
	v_pk_fma_f32 v[122:123], v[150:151], v[66:67], v[122:123] op_sel_hi:[1,0,1]
	v_pk_fma_f32 v[120:121], v[152:153], v[66:67], v[120:121] op_sel_hi:[1,0,1]
	v_pk_fma_f32 v[64:65], v[128:129], v[66:67], v[64:65] op_sel_hi:[1,0,1]
	v_pk_fma_f32 v[118:119], v[154:155], v[68:69], v[118:119] op_sel_hi:[1,0,1]
	v_pk_fma_f32 v[122:123], v[156:157], v[68:69], v[122:123] op_sel_hi:[1,0,1]
	v_pk_fma_f32 v[120:121], v[158:159], v[68:69], v[120:121] op_sel_hi:[1,0,1]
	v_pk_fma_f32 v[64:65], v[130:131], v[68:69], v[64:65] op_sel_hi:[1,0,1]
	v_pk_fma_f32 v[118:119], v[160:161], v[70:71], v[118:119] op_sel_hi:[1,0,1]
	v_pk_fma_f32 v[122:123], v[162:163], v[70:71], v[122:123] op_sel_hi:[1,0,1]
	v_pk_fma_f32 v[120:121], v[164:165], v[70:71], v[120:121] op_sel_hi:[1,0,1]
	v_pk_fma_f32 v[64:65], v[132:133], v[70:71], v[64:65] op_sel_hi:[1,0,1]
	s_waitcnt lgkmcnt(7)
	v_cvt_pk_f32_fp8_e32 v[206:207], v190
	v_cvt_pk_f32_fp8_sdwa v[208:209], v190 src0_sel:WORD_1
	v_cvt_pk_f32_fp8_e32 v[210:211], v191
	v_cvt_pk_f32_fp8_sdwa v[190:191], v191 src0_sel:WORD_1
	v_pk_fma_f32 v[118:119], v[166:167], v[72:73], v[118:119] op_sel_hi:[1,0,1]
	v_pk_fma_f32 v[122:123], v[168:169], v[72:73], v[122:123] op_sel_hi:[1,0,1]
	v_pk_fma_f32 v[120:121], v[170:171], v[72:73], v[120:121] op_sel_hi:[1,0,1]
	v_pk_fma_f32 v[64:65], v[134:135], v[72:73], v[64:65] op_sel_hi:[1,0,1]
	v_pk_fma_f32 v[118:119], v[172:173], v[74:75], v[118:119] op_sel_hi:[1,0,1]
	v_pk_fma_f32 v[122:123], v[174:175], v[74:75], v[122:123] op_sel_hi:[1,0,1]
	v_pk_fma_f32 v[120:121], v[176:177], v[74:75], v[120:121] op_sel_hi:[1,0,1]
	v_pk_fma_f32 v[64:65], v[136:137], v[74:75], v[64:65] op_sel_hi:[1,0,1]
	s_waitcnt lgkmcnt(6)
	v_cvt_pk_f32_fp8_e32 v[66:67], v192
	v_cvt_pk_f32_fp8_sdwa v[68:69], v192 src0_sel:WORD_1
	v_cvt_pk_f32_fp8_e32 v[70:71], v193
	v_cvt_pk_f32_fp8_sdwa v[72:73], v193 src0_sel:WORD_1
	s_waitcnt lgkmcnt(5)
	v_cvt_pk_f32_fp8_e32 v[74:75], v194
	v_cvt_pk_f32_fp8_sdwa v[124:125], v194 src0_sel:WORD_1
	v_pk_fma_f32 v[118:119], v[178:179], v[48:49], v[118:119] op_sel_hi:[1,0,1]
	v_pk_fma_f32 v[122:123], v[180:181], v[48:49], v[122:123] op_sel_hi:[1,0,1]
	v_pk_fma_f32 v[120:121], v[182:183], v[48:49], v[120:121] op_sel_hi:[1,0,1]
	v_pk_fma_f32 v[48:49], v[138:139], v[48:49], v[64:65] op_sel_hi:[1,0,1]
	v_pk_fma_f32 v[118:119], v[184:185], v[50:51], v[118:119] op_sel_hi:[1,0,1]
	v_pk_fma_f32 v[122:123], v[186:187], v[50:51], v[122:123] op_sel_hi:[1,0,1]
	v_pk_fma_f32 v[120:121], v[188:189], v[50:51], v[120:121] op_sel_hi:[1,0,1]
	v_pk_fma_f32 v[48:49], v[140:141], v[50:51], v[48:49] op_sel_hi:[1,0,1]
	v_pk_fma_f32 v[118:119], v[206:207], v[52:53], v[118:119] op_sel_hi:[1,0,1]
	v_pk_fma_f32 v[122:123], v[208:209], v[52:53], v[122:123] op_sel_hi:[1,0,1]
	v_pk_fma_f32 v[120:121], v[210:211], v[52:53], v[120:121] op_sel_hi:[1,0,1]
	v_pk_fma_f32 v[48:49], v[190:191], v[52:53], v[48:49] op_sel_hi:[1,0,1]
	v_cvt_pk_f32_fp8_e32 v[126:127], v195
	v_cvt_pk_f32_fp8_sdwa v[128:129], v195 src0_sel:WORD_1
	s_waitcnt lgkmcnt(4)
	v_cvt_pk_f32_fp8_e32 v[130:131], v196
	v_cvt_pk_f32_fp8_sdwa v[132:133], v196 src0_sel:WORD_1
	v_cvt_pk_f32_fp8_e32 v[134:135], v197
	v_cvt_pk_f32_fp8_sdwa v[136:137], v197 src0_sel:WORD_1
	s_waitcnt lgkmcnt(3)
	v_cvt_pk_f32_fp8_e32 v[142:143], v198
	v_cvt_pk_f32_fp8_sdwa v[144:145], v198 src0_sel:WORD_1
	v_cvt_pk_f32_fp8_e32 v[146:147], v199
	v_cvt_pk_f32_fp8_sdwa v[148:149], v199 src0_sel:WORD_1
	s_waitcnt lgkmcnt(2)
	v_cvt_pk_f32_fp8_e32 v[150:151], v200
	v_cvt_pk_f32_fp8_sdwa v[152:153], v200 src0_sel:WORD_1
	v_cvt_pk_f32_fp8_e32 v[154:155], v201
	v_cvt_pk_f32_fp8_sdwa v[156:157], v201 src0_sel:WORD_1
	s_waitcnt lgkmcnt(1)
	v_cvt_pk_f32_fp8_e32 v[158:159], v202
	v_cvt_pk_f32_fp8_sdwa v[160:161], v202 src0_sel:WORD_1
	v_cvt_pk_f32_fp8_e32 v[162:163], v203
	v_cvt_pk_f32_fp8_sdwa v[164:165], v203 src0_sel:WORD_1
	s_waitcnt lgkmcnt(0)
	v_cvt_pk_f32_fp8_e32 v[166:167], v204
	v_cvt_pk_f32_fp8_sdwa v[168:169], v204 src0_sel:WORD_1
	v_cvt_pk_f32_fp8_e32 v[170:171], v205
	v_cvt_pk_f32_fp8_sdwa v[172:173], v205 src0_sel:WORD_1
	s_setprio 0
	s_waitcnt vmcnt(40)
	v_and_b32_e32 v9, 0x1fff8, v46
	v_and_b32_e32 v11, 0x1fff8, v26
	v_and_b32_e32 v13, 0x1fff8, v28
	v_and_b32_e32 v15, 0x1fff8, v30
	ds_read_b64 v[50:51], v9
	ds_read_b64 v[52:53], v11
	ds_read_b64 v[64:65], v13
	ds_read_b64 v[138:139], v15
	v_and_b32_e32 v9, 0x1fff8, v4
	v_and_b32_e32 v11, 0x1fff8, v6
	v_and_b32_e32 v13, 0x1fff8, v8
	v_and_b32_e32 v15, 0x1fff8, v10
	ds_read_b64 v[140:141], v9
	ds_read_b64 v[174:175], v11
	ds_read_b64 v[176:177], v13
	ds_read_b64 v[178:179], v15
	s_setprio 1
	v_pk_fma_f32 v[66:67], v[66:67], v[32:33], v[118:119] op_sel_hi:[1,0,1]
	v_pk_fma_f32 v[68:69], v[68:69], v[32:33], v[122:123] op_sel_hi:[1,0,1]
	v_pk_fma_f32 v[70:71], v[70:71], v[32:33], v[120:121] op_sel_hi:[1,0,1]
	v_pk_fma_f32 v[32:33], v[72:73], v[32:33], v[48:49] op_sel_hi:[1,0,1]
	v_pk_fma_f32 v[66:67], v[74:75], v[34:35], v[66:67] op_sel_hi:[1,0,1]
	v_pk_fma_f32 v[68:69], v[124:125], v[34:35], v[68:69] op_sel_hi:[1,0,1]
	v_pk_fma_f32 v[70:71], v[126:127], v[34:35], v[70:71] op_sel_hi:[1,0,1]
	v_pk_fma_f32 v[32:33], v[128:129], v[34:35], v[32:33] op_sel_hi:[1,0,1]
	v_pk_fma_f32 v[66:67], v[130:131], v[36:37], v[66:67] op_sel_hi:[1,0,1]
	v_pk_fma_f32 v[68:69], v[132:133], v[36:37], v[68:69] op_sel_hi:[1,0,1]
	v_pk_fma_f32 v[70:71], v[134:135], v[36:37], v[70:71] op_sel_hi:[1,0,1]
	v_pk_fma_f32 v[32:33], v[136:137], v[36:37], v[32:33] op_sel_hi:[1,0,1]
	s_waitcnt lgkmcnt(7)
	v_cvt_pk_f32_fp8_e32 v[180:181], v50
	v_cvt_pk_f32_fp8_sdwa v[182:183], v50 src0_sel:WORD_1
	v_cvt_pk_f32_fp8_e32 v[184:185], v51
	v_cvt_pk_f32_fp8_sdwa v[50:51], v51 src0_sel:WORD_1
	v_pk_fma_f32 v[66:67], v[142:143], v[38:39], v[66:67] op_sel_hi:[1,0,1]
	v_pk_fma_f32 v[68:69], v[144:145], v[38:39], v[68:69] op_sel_hi:[1,0,1]
	v_pk_fma_f32 v[70:71], v[146:147], v[38:39], v[70:71] op_sel_hi:[1,0,1]
	v_pk_fma_f32 v[32:33], v[148:149], v[38:39], v[32:33] op_sel_hi:[1,0,1]
	s_waitcnt lgkmcnt(6)
	v_cvt_pk_f32_fp8_e32 v[186:187], v52
	v_cvt_pk_f32_fp8_sdwa v[188:189], v52 src0_sel:WORD_1
	v_cvt_pk_f32_fp8_e32 v[190:191], v53
	v_cvt_pk_f32_fp8_sdwa v[52:53], v53 src0_sel:WORD_1
	v_pk_fma_f32 v[66:67], v[150:151], v[40:41], v[66:67] op_sel_hi:[1,0,1]
	v_pk_fma_f32 v[68:69], v[152:153], v[40:41], v[68:69] op_sel_hi:[1,0,1]
	v_pk_fma_f32 v[70:71], v[154:155], v[40:41], v[70:71] op_sel_hi:[1,0,1]
	v_pk_fma_f32 v[32:33], v[156:157], v[40:41], v[32:33] op_sel_hi:[1,0,1]
	s_waitcnt lgkmcnt(5)
	v_cvt_pk_f32_fp8_e32 v[192:193], v64
	v_cvt_pk_f32_fp8_sdwa v[194:195], v64 src0_sel:WORD_1
	v_cvt_pk_f32_fp8_e32 v[196:197], v65
	v_cvt_pk_f32_fp8_sdwa v[64:65], v65 src0_sel:WORD_1
	v_pk_fma_f32 v[66:67], v[158:159], v[42:43], v[66:67] op_sel_hi:[1,0,1]
	v_pk_fma_f32 v[68:69], v[160:161], v[42:43], v[68:69] op_sel_hi:[1,0,1]
	v_pk_fma_f32 v[70:71], v[162:163], v[42:43], v[70:71] op_sel_hi:[1,0,1]
	v_pk_fma_f32 v[32:33], v[164:165], v[42:43], v[32:33] op_sel_hi:[1,0,1]
	s_waitcnt lgkmcnt(4)
	v_cvt_pk_f32_fp8_e32 v[198:199], v138
	v_cvt_pk_f32_fp8_sdwa v[200:201], v138 src0_sel:WORD_1
	v_cvt_pk_f32_fp8_e32 v[202:203], v139
	v_cvt_pk_f32_fp8_sdwa v[138:139], v139 src0_sel:WORD_1
	v_pk_fma_f32 v[66:67], v[166:167], v[44:45], v[66:67] op_sel_hi:[1,0,1]
	v_pk_fma_f32 v[68:69], v[168:169], v[44:45], v[68:69] op_sel_hi:[1,0,1]
	v_pk_fma_f32 v[70:71], v[170:171], v[44:45], v[70:71] op_sel_hi:[1,0,1]
	v_pk_fma_f32 v[32:33], v[172:173], v[44:45], v[32:33] op_sel_hi:[1,0,1]
	v_pk_fma_f32 v[66:67], v[180:181], v[46:47], v[66:67] op_sel_hi:[1,0,1]
	v_pk_fma_f32 v[68:69], v[182:183], v[46:47], v[68:69] op_sel_hi:[1,0,1]
	v_pk_fma_f32 v[70:71], v[184:185], v[46:47], v[70:71] op_sel_hi:[1,0,1]
	v_pk_fma_f32 v[32:33], v[50:51], v[46:47], v[32:33] op_sel_hi:[1,0,1]
	s_waitcnt lgkmcnt(3)
	v_cvt_pk_f32_fp8_e32 v[34:35], v140
	v_cvt_pk_f32_fp8_sdwa v[36:37], v140 src0_sel:WORD_1
	v_cvt_pk_f32_fp8_e32 v[38:39], v141
	v_cvt_pk_f32_fp8_sdwa v[40:41], v141 src0_sel:WORD_1
	s_waitcnt lgkmcnt(2)
	v_cvt_pk_f32_fp8_e32 v[42:43], v174
	v_cvt_pk_f32_fp8_sdwa v[44:45], v174 src0_sel:WORD_1
	v_cvt_pk_f32_fp8_e32 v[46:47], v175
	v_cvt_pk_f32_fp8_sdwa v[48:49], v175 src0_sel:WORD_1
	s_waitcnt lgkmcnt(1)
	v_cvt_pk_f32_fp8_e32 v[50:51], v176
	v_cvt_pk_f32_fp8_sdwa v[72:73], v176 src0_sel:WORD_1
	v_cvt_pk_f32_fp8_e32 v[74:75], v177
	v_cvt_pk_f32_fp8_sdwa v[118:119], v177 src0_sel:WORD_1
	s_waitcnt lgkmcnt(0)
	v_cvt_pk_f32_fp8_e32 v[120:121], v178
	v_cvt_pk_f32_fp8_sdwa v[122:123], v178 src0_sel:WORD_1
	v_cvt_pk_f32_fp8_e32 v[124:125], v179
	v_pk_fma_f32 v[66:67], v[186:187], v[26:27], v[66:67] op_sel_hi:[1,0,1]
	v_pk_fma_f32 v[68:69], v[188:189], v[26:27], v[68:69] op_sel_hi:[1,0,1]
	v_pk_fma_f32 v[70:71], v[190:191], v[26:27], v[70:71] op_sel_hi:[1,0,1]
	v_pk_fma_f32 v[26:27], v[52:53], v[26:27], v[32:33] op_sel_hi:[1,0,1]
	v_pk_fma_f32 v[66:67], v[192:193], v[28:29], v[66:67] op_sel_hi:[1,0,1]
	v_pk_fma_f32 v[68:69], v[194:195], v[28:29], v[68:69] op_sel_hi:[1,0,1]
	v_pk_fma_f32 v[70:71], v[196:197], v[28:29], v[70:71] op_sel_hi:[1,0,1]
	v_pk_fma_f32 v[26:27], v[64:65], v[28:29], v[26:27] op_sel_hi:[1,0,1]
	v_pk_fma_f32 v[66:67], v[198:199], v[30:31], v[66:67] op_sel_hi:[1,0,1]
	v_pk_fma_f32 v[68:69], v[200:201], v[30:31], v[68:69] op_sel_hi:[1,0,1]
	v_pk_fma_f32 v[70:71], v[202:203], v[30:31], v[70:71] op_sel_hi:[1,0,1]
	v_pk_fma_f32 v[26:27], v[138:139], v[30:31], v[26:27] op_sel_hi:[1,0,1]
	v_cvt_pk_f32_fp8_sdwa v[126:127], v179 src0_sel:WORD_1
	s_setprio 0
	s_waitcnt vmcnt(32)
	v_and_b32_e32 v9, 0x1fff8, v14
	v_and_b32_e32 v11, 0x1fff8, v18
	v_and_b32_e32 v13, 0x1fff8, v20
	v_and_b32_e32 v15, 0x1fff8, v22
	ds_read_b64 v[28:29], v9
	ds_read_b64 v[30:31], v11
	ds_read_b64 v[32:33], v13
	ds_read_b64 v[52:53], v15
	v_and_b32_e32 v9, 0x1fff8, v24
	v_and_b32_e32 v11, 0x1fff8, v12
	v_and_b32_e32 v13, 0x1fff8, v16
	v_and_b32_e32 v15, 0x1fff8, v7
	ds_read_b64 v[64:65], v9
	ds_read_b64 v[128:129], v11
	ds_read_b64 v[130:131], v13
	ds_read_b64 v[132:133], v15
	s_setprio 1
	s_waitcnt lgkmcnt(7)
	v_cvt_pk_f32_fp8_e32 v[134:135], v28
	v_pk_fma_f32 v[34:35], v[34:35], v[4:5], v[66:67] op_sel_hi:[1,0,1]
	s_waitcnt lgkmcnt(6)
	v_cvt_pk_f32_fp8_e32 v[140:141], v30
	v_pk_fma_f32 v[34:35], v[42:43], v[6:7], v[34:35] op_sel_hi:[1,0,1]
	s_waitcnt lgkmcnt(5)
	v_cvt_pk_f32_fp8_e32 v[146:147], v32
	v_pk_fma_f32 v[34:35], v[50:51], v[8:9], v[34:35] op_sel_hi:[1,0,1]
	s_waitcnt lgkmcnt(4)
	v_cvt_pk_f32_fp8_e32 v[152:153], v52
	v_pk_fma_f32 v[34:35], v[120:121], v[10:11], v[34:35] op_sel_hi:[1,0,1]
	s_waitcnt lgkmcnt(3)
	v_cvt_pk_f32_fp8_e32 v[158:159], v64
	v_pk_fma_f32 v[34:35], v[134:135], v[14:15], v[34:35] op_sel_hi:[1,0,1]
	s_waitcnt lgkmcnt(2)
	v_cvt_pk_f32_fp8_e32 v[164:165], v128
	v_pk_fma_f32 v[34:35], v[140:141], v[18:19], v[34:35] op_sel_hi:[1,0,1]
	s_waitcnt lgkmcnt(1)
	v_cvt_pk_f32_fp8_e32 v[170:171], v130
	v_pk_fma_f32 v[34:35], v[146:147], v[20:21], v[34:35] op_sel_hi:[1,0,1]
	v_cvt_pk_f32_fp8_sdwa v[136:137], v28 src0_sel:WORD_1
	v_pk_fma_f32 v[34:35], v[152:153], v[22:23], v[34:35] op_sel_hi:[1,0,1]
	v_cvt_pk_f32_fp8_sdwa v[142:143], v30 src0_sel:WORD_1
	v_pk_fma_f32 v[34:35], v[158:159], v[24:25], v[34:35] op_sel_hi:[1,0,1]
	v_cvt_pk_f32_fp8_sdwa v[148:149], v32 src0_sel:WORD_1
	v_pk_fma_f32 v[34:35], v[164:165], v[12:13], v[34:35] op_sel_hi:[1,0,1]
	v_cvt_pk_f32_fp8_sdwa v[154:155], v52 src0_sel:WORD_1
	v_pk_fma_f32 v[120:121], v[170:171], v[16:17], v[34:35] op_sel_hi:[1,0,1]
	v_pk_fma_f32 v[34:35], v[36:37], v[4:5], v[68:69] op_sel_hi:[1,0,1]
	v_cvt_pk_f32_fp8_sdwa v[160:161], v64 src0_sel:WORD_1
	v_pk_fma_f32 v[34:35], v[44:45], v[6:7], v[34:35] op_sel_hi:[1,0,1]
	v_cvt_pk_f32_fp8_sdwa v[166:167], v128 src0_sel:WORD_1
	v_pk_fma_f32 v[34:35], v[72:73], v[8:9], v[34:35] op_sel_hi:[1,0,1]
	v_cvt_pk_f32_fp8_sdwa v[172:173], v130 src0_sel:WORD_1
	v_pk_fma_f32 v[34:35], v[122:123], v[10:11], v[34:35] op_sel_hi:[1,0,1]
	v_cvt_pk_f32_fp8_e32 v[138:139], v29
	v_pk_fma_f32 v[34:35], v[136:137], v[14:15], v[34:35] op_sel_hi:[1,0,1]
	v_cvt_pk_f32_fp8_sdwa v[28:29], v29 src0_sel:WORD_1
	v_pk_fma_f32 v[34:35], v[142:143], v[18:19], v[34:35] op_sel_hi:[1,0,1]
	v_cvt_pk_f32_fp8_e32 v[144:145], v31
	v_pk_fma_f32 v[34:35], v[148:149], v[20:21], v[34:35] op_sel_hi:[1,0,1]
	v_pk_fma_f32 v[26:27], v[40:41], v[4:5], v[26:27] op_sel_hi:[1,0,1]
	v_pk_fma_f32 v[34:35], v[154:155], v[22:23], v[34:35] op_sel_hi:[1,0,1]
	v_cvt_pk_f32_fp8_sdwa v[30:31], v31 src0_sel:WORD_1
	v_pk_fma_f32 v[34:35], v[160:161], v[24:25], v[34:35] op_sel_hi:[1,0,1]
	v_cvt_pk_f32_fp8_e32 v[150:151], v33
	v_pk_fma_f32 v[34:35], v[166:167], v[12:13], v[34:35] op_sel_hi:[1,0,1]
	v_pk_fma_f32 v[26:27], v[48:49], v[6:7], v[26:27] op_sel_hi:[1,0,1]
	v_pk_fma_f32 v[122:123], v[172:173], v[16:17], v[34:35] op_sel_hi:[1,0,1]
	v_pk_fma_f32 v[34:35], v[38:39], v[4:5], v[70:71] op_sel_hi:[1,0,1]
	v_cvt_pk_f32_fp8_sdwa v[32:33], v33 src0_sel:WORD_1
	v_pk_fma_f32 v[34:35], v[46:47], v[6:7], v[34:35] op_sel_hi:[1,0,1]
	v_cvt_pk_f32_fp8_e32 v[156:157], v53
	v_pk_fma_f32 v[34:35], v[74:75], v[8:9], v[34:35] op_sel_hi:[1,0,1]
	v_pk_fma_f32 v[8:9], v[118:119], v[8:9], v[26:27] op_sel_hi:[1,0,1]
	v_pk_fma_f32 v[34:35], v[124:125], v[10:11], v[34:35] op_sel_hi:[1,0,1]
	v_cvt_pk_f32_fp8_sdwa v[52:53], v53 src0_sel:WORD_1
	v_cvt_pk_f32_fp8_e32 v[162:163], v65
	v_pk_fma_f32 v[34:35], v[138:139], v[14:15], v[34:35] op_sel_hi:[1,0,1]
	v_pk_fma_f32 v[8:9], v[126:127], v[10:11], v[8:9] op_sel_hi:[1,0,1]
	v_cvt_pk_f32_fp8_sdwa v[64:65], v65 src0_sel:WORD_1
	v_cvt_pk_f32_fp8_e32 v[168:169], v129
	v_pk_fma_f32 v[34:35], v[144:145], v[18:19], v[34:35] op_sel_hi:[1,0,1]
	v_pk_fma_f32 v[8:9], v[28:29], v[14:15], v[8:9] op_sel_hi:[1,0,1]
	v_cvt_pk_f32_fp8_sdwa v[128:129], v129 src0_sel:WORD_1
	v_cvt_pk_f32_fp8_e32 v[174:175], v131
	v_pk_fma_f32 v[34:35], v[150:151], v[20:21], v[34:35] op_sel_hi:[1,0,1]
	v_pk_fma_f32 v[8:9], v[30:31], v[18:19], v[8:9] op_sel_hi:[1,0,1]
	v_cvt_pk_f32_fp8_sdwa v[130:131], v131 src0_sel:WORD_1
	v_pk_fma_f32 v[34:35], v[156:157], v[22:23], v[34:35] op_sel_hi:[1,0,1]
	v_pk_fma_f32 v[8:9], v[32:33], v[20:21], v[8:9] op_sel_hi:[1,0,1]
	s_waitcnt lgkmcnt(0)
	v_cvt_pk_f32_fp8_e32 v[118:119], v132
	v_pk_fma_f32 v[34:35], v[162:163], v[24:25], v[34:35] op_sel_hi:[1,0,1]
	v_pk_fma_f32 v[8:9], v[52:53], v[22:23], v[8:9] op_sel_hi:[1,0,1]
	v_pk_fma_f32 v[34:35], v[168:169], v[12:13], v[34:35] op_sel_hi:[1,0,1]
	v_pk_fma_f32 v[8:9], v[64:65], v[24:25], v[8:9] op_sel_hi:[1,0,1]
	v_pk_fma_f32 v[124:125], v[174:175], v[16:17], v[34:35] op_sel_hi:[1,0,1]
	v_pk_fma_f32 v[8:9], v[128:129], v[12:13], v[8:9] op_sel_hi:[1,0,1]
	v_cvt_pk_f32_fp8_sdwa v[126:127], v132 src0_sel:WORD_1
	v_cvt_pk_f32_fp8_e32 v[134:135], v133
	v_cvt_pk_f32_fp8_sdwa v[132:133], v133 src0_sel:WORD_1
	v_pk_fma_f32 v[128:129], v[130:131], v[16:17], v[8:9] op_sel_hi:[1,0,1]
	v_mov_b32_e32 v130, v7
	s_setprio 0
	s_add_i32 s18, s18, 2
	s_cmp_gt_u32 s17, 61
	s_cselect_b64 s[10:11], -1, 0
	s_cmp_lt_u32 s17, 62
	s_cselect_b32 s19, s18, 63
	s_lshl_b32 s20, s19, 1
	s_and_b32 s20, s20, 0xf8
	s_add_i32 s20, s20, s4
	s_ashr_i32 s21, s20, 31
	s_lshl_b64 s[20:21], s[20:21], 15
	s_add_u32 s20, s12, s20
	s_addc_u32 s21, s13, s21
	s_lshl_b32 s19, s19, 13
	s_and_b32 s19, s19, 0x6000
	s_add_u32 s20, s20, s19
	s_addc_u32 s21, s21, 0
	s_add_u32 s66, s20, s5
	s_addc_u32 s67, s21, 0
	global_load_dword v64, v2, s[20:21]
	global_load_dword v66, v2, s[20:21] offset:256
	global_load_dword v68, v2, s[20:21] offset:512
	global_load_dword v70, v2, s[20:21] offset:768
	global_load_dword v72, v2, s[20:21] offset:1024
	global_load_dword v74, v2, s[20:21] offset:1280
	global_load_dword v48, v2, s[20:21] offset:1536
	global_load_dword v50, v2, s[20:21] offset:1792
	global_load_dword v52, v2, s[20:21] offset:2048
	global_load_dword v32, v2, s[20:21] offset:2304
	global_load_dword v34, v2, s[20:21] offset:2560
	global_load_dword v36, v2, s[20:21] offset:2816
	global_load_dword v38, v2, s[20:21] offset:3072
	global_load_dword v40, v2, s[20:21] offset:3328
	global_load_dword v42, v2, s[20:21] offset:3584
	global_load_dword v44, v2, s[20:21] offset:3840
	global_load_dword v46, v2, s[66:67]
	global_load_dword v26, v2, s[66:67] offset:256
	global_load_dword v28, v2, s[66:67] offset:512
	global_load_dword v30, v2, s[66:67] offset:768
	global_load_dword v4, v2, s[66:67] offset:1024
	global_load_dword v6, v2, s[66:67] offset:1280
	global_load_dword v8, v2, s[66:67] offset:1536
	global_load_dword v10, v2, s[66:67] offset:1792
	global_load_dword v14, v2, s[66:67] offset:2048
	global_load_dword v18, v2, s[66:67] offset:2304
	global_load_dword v20, v2, s[66:67] offset:2560
	global_load_dword v22, v2, s[66:67] offset:2816
	global_load_dword v24, v2, s[66:67] offset:3072
	global_load_dword v12, v2, s[66:67] offset:3328
	global_load_dword v16, v2, s[66:67] offset:3584
	global_load_dword v7, v2, s[66:67] offset:3840
	s_waitcnt vmcnt(55)
	v_and_b32_e32 v9, 0x1fff8, v116
	v_and_b32_e32 v11, 0x1fff8, v104
	v_and_b32_e32 v13, 0x1fff8, v106
	v_and_b32_e32 v15, 0x1fff8, v108
	ds_read_b64 v[136:137], v9
	ds_read_b64 v[138:139], v11
	ds_read_b64 v[140:141], v13
	ds_read_b64 v[142:143], v15
	v_and_b32_e32 v9, 0x1fff8, v110
	v_and_b32_e32 v11, 0x1fff8, v112
	v_and_b32_e32 v13, 0x1fff8, v114
	v_and_b32_e32 v15, 0x1fff8, v98
	ds_read_b64 v[144:145], v9
	ds_read_b64 v[146:147], v11
	ds_read_b64 v[148:149], v13
	ds_read_b64 v[150:151], v15
	s_setprio 1
	s_waitcnt lgkmcnt(7)
	v_cvt_pk_f32_fp8_e32 v[152:153], v136
	v_cvt_pk_f32_fp8_sdwa v[154:155], v136 src0_sel:WORD_1
	v_cvt_pk_f32_fp8_e32 v[156:157], v137
	v_cvt_pk_f32_fp8_sdwa v[136:137], v137 src0_sel:WORD_1
	s_waitcnt lgkmcnt(6)
	v_cvt_pk_f32_fp8_e32 v[158:159], v138
	v_cvt_pk_f32_fp8_sdwa v[160:161], v138 src0_sel:WORD_1
	v_cvt_pk_f32_fp8_e32 v[162:163], v139
	v_cvt_pk_f32_fp8_sdwa v[138:139], v139 src0_sel:WORD_1
	s_waitcnt lgkmcnt(5)
	v_cvt_pk_f32_fp8_e32 v[164:165], v140
	v_cvt_pk_f32_fp8_sdwa v[166:167], v140 src0_sel:WORD_1
	v_cvt_pk_f32_fp8_e32 v[168:169], v141
	v_cvt_pk_f32_fp8_sdwa v[140:141], v141 src0_sel:WORD_1
	s_waitcnt lgkmcnt(4)
	v_cvt_pk_f32_fp8_e32 v[170:171], v142
	v_cvt_pk_f32_fp8_sdwa v[172:173], v142 src0_sel:WORD_1
	v_cvt_pk_f32_fp8_e32 v[174:175], v143
	v_cvt_pk_f32_fp8_sdwa v[142:143], v143 src0_sel:WORD_1
	s_waitcnt lgkmcnt(3)
	v_cvt_pk_f32_fp8_e32 v[176:177], v144
	v_cvt_pk_f32_fp8_sdwa v[178:179], v144 src0_sel:WORD_1
	v_cvt_pk_f32_fp8_e32 v[180:181], v145
	v_cvt_pk_f32_fp8_sdwa v[144:145], v145 src0_sel:WORD_1
	s_waitcnt lgkmcnt(2)
	v_cvt_pk_f32_fp8_e32 v[182:183], v146
	v_cvt_pk_f32_fp8_sdwa v[184:185], v146 src0_sel:WORD_1
	v_cvt_pk_f32_fp8_e32 v[186:187], v147
	v_cvt_pk_f32_fp8_sdwa v[146:147], v147 src0_sel:WORD_1
	s_waitcnt lgkmcnt(1)
	v_cvt_pk_f32_fp8_e32 v[188:189], v148
	v_cvt_pk_f32_fp8_sdwa v[190:191], v148 src0_sel:WORD_1
	v_cvt_pk_f32_fp8_e32 v[192:193], v149
	v_cvt_pk_f32_fp8_sdwa v[148:149], v149 src0_sel:WORD_1
	s_waitcnt lgkmcnt(0)
	v_cvt_pk_f32_fp8_e32 v[194:195], v150
	v_cvt_pk_f32_fp8_sdwa v[196:197], v150 src0_sel:WORD_1
	v_cvt_pk_f32_fp8_e32 v[198:199], v151
	v_cvt_pk_f32_fp8_sdwa v[150:151], v151 src0_sel:WORD_1
	s_setprio 0
	v_and_b32_e32 v9, 0x1fff8, v100
	s_waitcnt vmcnt(48)
	v_and_b32_e32 v11, 0x1fff8, v102
	v_and_b32_e32 v13, 0x1fff8, v78
	v_and_b32_e32 v15, 0x1fff8, v80
	ds_read_b64 v[200:201], v9
	ds_read_b64 v[202:203], v11
	ds_read_b64 v[204:205], v13
	ds_read_b64 v[206:207], v15
	v_and_b32_e32 v9, 0x1fff8, v82
	v_and_b32_e32 v11, 0x1fff8, v84
	v_and_b32_e32 v13, 0x1fff8, v86
	v_and_b32_e32 v15, 0x1fff8, v88
	ds_read_b64 v[208:209], v9
	ds_read_b64 v[210:211], v11
	ds_read_b64 v[212:213], v13
	ds_read_b64 v[214:215], v15
	s_setprio 1
	v_pk_fma_f32 v[118:119], v[118:119], v[130:131], v[120:121] op_sel_hi:[1,0,1]
	v_pk_fma_f32 v[120:121], v[126:127], v[130:131], v[122:123] op_sel_hi:[1,0,1]
	v_pk_fma_f32 v[122:123], v[134:135], v[130:131], v[124:125] op_sel_hi:[1,0,1]
	v_pk_fma_f32 v[118:119], v[152:153], v[116:117], v[118:119] op_sel_hi:[1,0,1]
	v_pk_fma_f32 v[120:121], v[154:155], v[116:117], v[120:121] op_sel_hi:[1,0,1]
	v_pk_fma_f32 v[122:123], v[156:157], v[116:117], v[122:123] op_sel_hi:[1,0,1]
	v_pk_fma_f32 v[124:125], v[132:133], v[130:131], v[128:129] op_sel_hi:[1,0,1]
	v_pk_fma_f32 v[118:119], v[158:159], v[104:105], v[118:119] op_sel_hi:[1,0,1]
	v_pk_fma_f32 v[120:121], v[160:161], v[104:105], v[120:121] op_sel_hi:[1,0,1]
	v_pk_fma_f32 v[122:123], v[162:163], v[104:105], v[122:123] op_sel_hi:[1,0,1]
	v_pk_fma_f32 v[116:117], v[136:137], v[116:117], v[124:125] op_sel_hi:[1,0,1]
	v_pk_fma_f32 v[118:119], v[164:165], v[106:107], v[118:119] op_sel_hi:[1,0,1]
	v_pk_fma_f32 v[120:121], v[166:167], v[106:107], v[120:121] op_sel_hi:[1,0,1]
	v_pk_fma_f32 v[122:123], v[168:169], v[106:107], v[122:123] op_sel_hi:[1,0,1]
	v_pk_fma_f32 v[104:105], v[138:139], v[104:105], v[116:117] op_sel_hi:[1,0,1]
	v_pk_fma_f32 v[118:119], v[170:171], v[108:109], v[118:119] op_sel_hi:[1,0,1]
	v_pk_fma_f32 v[120:121], v[172:173], v[108:109], v[120:121] op_sel_hi:[1,0,1]
	v_pk_fma_f32 v[122:123], v[174:175], v[108:109], v[122:123] op_sel_hi:[1,0,1]
	v_pk_fma_f32 v[104:105], v[140:141], v[106:107], v[104:105] op_sel_hi:[1,0,1]
	s_waitcnt lgkmcnt(7)
	v_cvt_pk_f32_fp8_e32 v[216:217], v200
	v_cvt_pk_f32_fp8_sdwa v[218:219], v200 src0_sel:WORD_1
	v_cvt_pk_f32_fp8_e32 v[220:221], v201
	v_pk_fma_f32 v[118:119], v[176:177], v[110:111], v[118:119] op_sel_hi:[1,0,1]
	v_pk_fma_f32 v[120:121], v[178:179], v[110:111], v[120:121] op_sel_hi:[1,0,1]
	v_pk_fma_f32 v[122:123], v[180:181], v[110:111], v[122:123] op_sel_hi:[1,0,1]
	v_pk_fma_f32 v[104:105], v[142:143], v[108:109], v[104:105] op_sel_hi:[1,0,1]
	v_cvt_pk_f32_fp8_sdwa v[200:201], v201 src0_sel:WORD_1
	s_waitcnt lgkmcnt(6)
	v_cvt_pk_f32_fp8_e32 v[222:223], v202
	v_cvt_pk_f32_fp8_sdwa v[224:225], v202 src0_sel:WORD_1
	v_cvt_pk_f32_fp8_e32 v[226:227], v203
	v_pk_fma_f32 v[118:119], v[182:183], v[112:113], v[118:119] op_sel_hi:[1,0,1]
	v_pk_fma_f32 v[120:121], v[184:185], v[112:113], v[120:121] op_sel_hi:[1,0,1]
	v_pk_fma_f32 v[122:123], v[186:187], v[112:113], v[122:123] op_sel_hi:[1,0,1]
	v_pk_fma_f32 v[104:105], v[144:145], v[110:111], v[104:105] op_sel_hi:[1,0,1]
	v_cvt_pk_f32_fp8_sdwa v[202:203], v203 src0_sel:WORD_1
	v_pk_fma_f32 v[118:119], v[188:189], v[114:115], v[118:119] op_sel_hi:[1,0,1]
	v_pk_fma_f32 v[120:121], v[190:191], v[114:115], v[120:121] op_sel_hi:[1,0,1]
	v_pk_fma_f32 v[122:123], v[192:193], v[114:115], v[122:123] op_sel_hi:[1,0,1]
	v_pk_fma_f32 v[104:105], v[146:147], v[112:113], v[104:105] op_sel_hi:[1,0,1]
	s_waitcnt lgkmcnt(4)
	v_cvt_pk_f32_fp8_e32 v[124:125], v207
	v_pk_fma_f32 v[118:119], v[194:195], v[98:99], v[118:119] op_sel_hi:[1,0,1]
	v_pk_fma_f32 v[120:121], v[196:197], v[98:99], v[120:121] op_sel_hi:[1,0,1]
	v_pk_fma_f32 v[122:123], v[198:199], v[98:99], v[122:123] op_sel_hi:[1,0,1]
	v_pk_fma_f32 v[104:105], v[148:149], v[114:115], v[104:105] op_sel_hi:[1,0,1]
	v_pk_fma_f32 v[118:119], v[216:217], v[100:101], v[118:119] op_sel_hi:[1,0,1]
	v_pk_fma_f32 v[120:121], v[218:219], v[100:101], v[120:121] op_sel_hi:[1,0,1]
	v_pk_fma_f32 v[122:123], v[220:221], v[100:101], v[122:123] op_sel_hi:[1,0,1]
	v_pk_fma_f32 v[98:99], v[150:151], v[98:99], v[104:105] op_sel_hi:[1,0,1]
	v_pk_fma_f32 v[118:119], v[222:223], v[102:103], v[118:119] op_sel_hi:[1,0,1]
	v_pk_fma_f32 v[120:121], v[224:225], v[102:103], v[120:121] op_sel_hi:[1,0,1]
	v_pk_fma_f32 v[122:123], v[226:227], v[102:103], v[122:123] op_sel_hi:[1,0,1]
	v_pk_fma_f32 v[98:99], v[200:201], v[100:101], v[98:99] op_sel_hi:[1,0,1]
	v_cvt_pk_f32_fp8_e32 v[106:107], v204
	v_cvt_pk_f32_fp8_sdwa v[108:109], v204 src0_sel:WORD_1
	v_cvt_pk_f32_fp8_e32 v[110:111], v205
	v_cvt_pk_f32_fp8_sdwa v[112:113], v205 src0_sel:WORD_1
	v_cvt_pk_f32_fp8_e32 v[114:115], v206
	v_cvt_pk_f32_fp8_sdwa v[116:117], v206 src0_sel:WORD_1
	v_cvt_pk_f32_fp8_sdwa v[126:127], v207 src0_sel:WORD_1
	s_waitcnt lgkmcnt(3)
	v_cvt_pk_f32_fp8_e32 v[128:129], v208
	v_cvt_pk_f32_fp8_sdwa v[130:131], v208 src0_sel:WORD_1
	v_cvt_pk_f32_fp8_e32 v[132:133], v209
	v_cvt_pk_f32_fp8_sdwa v[134:135], v209 src0_sel:WORD_1
	s_waitcnt lgkmcnt(2)
	v_cvt_pk_f32_fp8_e32 v[136:137], v210
	v_cvt_pk_f32_fp8_sdwa v[138:139], v210 src0_sel:WORD_1
	v_cvt_pk_f32_fp8_e32 v[140:141], v211
	v_cvt_pk_f32_fp8_sdwa v[142:143], v211 src0_sel:WORD_1
	s_waitcnt lgkmcnt(1)
	v_cvt_pk_f32_fp8_e32 v[144:145], v212
	v_cvt_pk_f32_fp8_sdwa v[146:147], v212 src0_sel:WORD_1
	v_cvt_pk_f32_fp8_e32 v[148:149], v213
	v_cvt_pk_f32_fp8_sdwa v[152:153], v213 src0_sel:WORD_1
	s_waitcnt lgkmcnt(0)
	v_cvt_pk_f32_fp8_e32 v[154:155], v214
	v_cvt_pk_f32_fp8_sdwa v[156:157], v214 src0_sel:WORD_1
	v_cvt_pk_f32_fp8_e32 v[158:159], v215
	v_cvt_pk_f32_fp8_sdwa v[160:161], v215 src0_sel:WORD_1
	v_pk_fma_f32 v[98:99], v[202:203], v[102:103], v[98:99] op_sel_hi:[1,0,1]
	s_setprio 0
	s_waitcnt vmcnt(40)
	v_and_b32_e32 v9, 0x1fff8, v90
	v_and_b32_e32 v11, 0x1fff8, v92
	v_and_b32_e32 v13, 0x1fff8, v94
	v_and_b32_e32 v15, 0x1fff8, v96
	ds_read_b64 v[100:101], v9
	ds_read_b64 v[102:103], v11
	ds_read_b64 v[104:105], v13
	ds_read_b64 v[150:151], v15
	v_and_b32_e32 v9, 0x1fff8, v76
	v_and_b32_e32 v11, 0x1fff8, v77
	v_and_b32_e32 v13, 0x1fff8, v56
	v_and_b32_e32 v15, 0x1fff8, v57
	ds_read_b64 v[162:163], v9
	ds_read_b64 v[164:165], v11
	ds_read_b64 v[166:167], v13
	ds_read_b64 v[168:169], v15
	s_setprio 1
	v_pk_fma_f32 v[106:107], v[106:107], v[78:79], v[118:119] op_sel_hi:[1,0,1]
	v_pk_fma_f32 v[108:109], v[108:109], v[78:79], v[120:121] op_sel_hi:[1,0,1]
	v_pk_fma_f32 v[110:111], v[110:111], v[78:79], v[122:123] op_sel_hi:[1,0,1]
	v_pk_fma_f32 v[78:79], v[112:113], v[78:79], v[98:99] op_sel_hi:[1,0,1]
	v_pk_fma_f32 v[106:107], v[114:115], v[80:81], v[106:107] op_sel_hi:[1,0,1]
	v_pk_fma_f32 v[108:109], v[116:117], v[80:81], v[108:109] op_sel_hi:[1,0,1]
	v_pk_fma_f32 v[110:111], v[124:125], v[80:81], v[110:111] op_sel_hi:[1,0,1]
	v_pk_fma_f32 v[78:79], v[126:127], v[80:81], v[78:79] op_sel_hi:[1,0,1]
	s_waitcnt lgkmcnt(7)
	v_cvt_pk_f32_fp8_e32 v[170:171], v100
	v_cvt_pk_f32_fp8_sdwa v[172:173], v100 src0_sel:WORD_1
	v_cvt_pk_f32_fp8_e32 v[174:175], v101
	v_cvt_pk_f32_fp8_sdwa v[100:101], v101 src0_sel:WORD_1
	v_pk_fma_f32 v[106:107], v[128:129], v[82:83], v[106:107] op_sel_hi:[1,0,1]
	v_pk_fma_f32 v[108:109], v[130:131], v[82:83], v[108:109] op_sel_hi:[1,0,1]
	v_pk_fma_f32 v[110:111], v[132:133], v[82:83], v[110:111] op_sel_hi:[1,0,1]
	v_pk_fma_f32 v[78:79], v[134:135], v[82:83], v[78:79] op_sel_hi:[1,0,1]
	s_waitcnt lgkmcnt(6)
	v_cvt_pk_f32_fp8_e32 v[176:177], v102
	v_cvt_pk_f32_fp8_sdwa v[178:179], v102 src0_sel:WORD_1
	v_cvt_pk_f32_fp8_e32 v[180:181], v103
	v_cvt_pk_f32_fp8_sdwa v[102:103], v103 src0_sel:WORD_1
	v_pk_fma_f32 v[106:107], v[136:137], v[84:85], v[106:107] op_sel_hi:[1,0,1]
	v_pk_fma_f32 v[108:109], v[138:139], v[84:85], v[108:109] op_sel_hi:[1,0,1]
	v_pk_fma_f32 v[110:111], v[140:141], v[84:85], v[110:111] op_sel_hi:[1,0,1]
	v_pk_fma_f32 v[78:79], v[142:143], v[84:85], v[78:79] op_sel_hi:[1,0,1]
	s_waitcnt lgkmcnt(5)
	v_cvt_pk_f32_fp8_e32 v[182:183], v104
	v_cvt_pk_f32_fp8_sdwa v[184:185], v104 src0_sel:WORD_1
	v_cvt_pk_f32_fp8_e32 v[186:187], v105
	v_cvt_pk_f32_fp8_sdwa v[104:105], v105 src0_sel:WORD_1
	v_pk_fma_f32 v[106:107], v[144:145], v[86:87], v[106:107] op_sel_hi:[1,0,1]
	v_pk_fma_f32 v[108:109], v[146:147], v[86:87], v[108:109] op_sel_hi:[1,0,1]
	v_pk_fma_f32 v[110:111], v[148:149], v[86:87], v[110:111] op_sel_hi:[1,0,1]
	v_pk_fma_f32 v[78:79], v[152:153], v[86:87], v[78:79] op_sel_hi:[1,0,1]
	v_pk_fma_f32 v[106:107], v[154:155], v[88:89], v[106:107] op_sel_hi:[1,0,1]
	v_pk_fma_f32 v[108:109], v[156:157], v[88:89], v[108:109] op_sel_hi:[1,0,1]
	v_pk_fma_f32 v[110:111], v[158:159], v[88:89], v[110:111] op_sel_hi:[1,0,1]
	v_pk_fma_f32 v[78:79], v[160:161], v[88:89], v[78:79] op_sel_hi:[1,0,1]
	s_waitcnt lgkmcnt(3)
	v_cvt_pk_f32_fp8_e32 v[194:195], v162
	v_cvt_pk_f32_fp8_sdwa v[196:197], v162 src0_sel:WORD_1
	v_cvt_pk_f32_fp8_e32 v[198:199], v163
	v_cvt_pk_f32_fp8_sdwa v[162:163], v163 src0_sel:WORD_1
	s_waitcnt lgkmcnt(2)
	v_cvt_pk_f32_fp8_e32 v[200:201], v164
	v_cvt_pk_f32_fp8_sdwa v[202:203], v164 src0_sel:WORD_1
	v_cvt_pk_f32_fp8_e32 v[204:205], v165
	v_cvt_pk_f32_fp8_sdwa v[164:165], v165 src0_sel:WORD_1
	v_pk_fma_f32 v[106:107], v[170:171], v[90:91], v[106:107] op_sel_hi:[1,0,1]
	v_pk_fma_f32 v[108:109], v[172:173], v[90:91], v[108:109] op_sel_hi:[1,0,1]
	v_pk_fma_f32 v[110:111], v[174:175], v[90:91], v[110:111] op_sel_hi:[1,0,1]
	v_pk_fma_f32 v[78:79], v[100:101], v[90:91], v[78:79] op_sel_hi:[1,0,1]
	v_pk_fma_f32 v[106:107], v[176:177], v[92:93], v[106:107] op_sel_hi:[1,0,1]
	v_pk_fma_f32 v[108:109], v[178:179], v[92:93], v[108:109] op_sel_hi:[1,0,1]
	v_pk_fma_f32 v[110:111], v[180:181], v[92:93], v[110:111] op_sel_hi:[1,0,1]
	v_pk_fma_f32 v[78:79], v[102:103], v[92:93], v[78:79] op_sel_hi:[1,0,1]
	v_cvt_pk_f32_fp8_e32 v[188:189], v150
	v_cvt_pk_f32_fp8_sdwa v[190:191], v150 src0_sel:WORD_1
	v_cvt_pk_f32_fp8_e32 v[192:193], v151
	v_cvt_pk_f32_fp8_sdwa v[150:151], v151 src0_sel:WORD_1
	v_pk_fma_f32 v[106:107], v[182:183], v[94:95], v[106:107] op_sel_hi:[1,0,1]
	v_pk_fma_f32 v[108:109], v[184:185], v[94:95], v[108:109] op_sel_hi:[1,0,1]
	v_pk_fma_f32 v[110:111], v[186:187], v[94:95], v[110:111] op_sel_hi:[1,0,1]
	v_pk_fma_f32 v[78:79], v[104:105], v[94:95], v[78:79] op_sel_hi:[1,0,1]
	s_waitcnt lgkmcnt(1)
	v_cvt_pk_f32_fp8_sdwa v[88:89], v167 src0_sel:WORD_1
	s_waitcnt lgkmcnt(0)
	v_cvt_pk_f32_fp8_sdwa v[94:95], v169 src0_sel:WORD_1
	v_pk_fma_f32 v[78:79], v[162:163], v[76:77], v[78:79] op_sel_hi:[1,0,1]
	v_pk_fma_f32 v[106:107], v[188:189], v[96:97], v[106:107] op_sel_hi:[1,0,1]
	v_pk_fma_f32 v[108:109], v[190:191], v[96:97], v[108:109] op_sel_hi:[1,0,1]
	v_pk_fma_f32 v[110:111], v[192:193], v[96:97], v[110:111] op_sel_hi:[1,0,1]
	v_pk_fma_f32 v[78:79], v[150:151], v[96:97], v[78:79] op_sel_hi:[1,0,1]
	v_pk_fma_f32 v[78:79], v[88:89], v[56:57], v[78:79] op_sel_hi:[1,0,1]
	v_pk_fma_f32 v[106:107], v[194:195], v[76:77], v[106:107] op_sel_hi:[1,0,1]
	v_pk_fma_f32 v[108:109], v[196:197], v[76:77], v[108:109] op_sel_hi:[1,0,1]
	v_pk_fma_f32 v[110:111], v[198:199], v[76:77], v[110:111] op_sel_hi:[1,0,1]
	v_mov_b32_e32 v76, v77
	v_pk_fma_f32 v[78:79], v[164:165], v[76:77], v[78:79] op_sel:[0,1,0] op_sel_hi:[1,1,1]
	v_cvt_pk_f32_fp8_e32 v[82:83], v166
	v_cvt_pk_f32_fp8_sdwa v[84:85], v166 src0_sel:WORD_1
	v_cvt_pk_f32_fp8_e32 v[86:87], v167
	v_cvt_pk_f32_fp8_e32 v[90:91], v168
	v_cvt_pk_f32_fp8_sdwa v[92:93], v168 src0_sel:WORD_1
	v_cvt_pk_f32_fp8_e32 v[96:97], v169
	v_pk_fma_f32 v[78:79], v[94:95], v[56:57], v[78:79] op_sel:[0,1,0] op_sel_hi:[1,1,1]
	s_setprio 0
	s_waitcnt vmcnt(32)
	v_and_b32_e32 v9, 0x1fff8, v58
	v_and_b32_e32 v11, 0x1fff8, v59
	v_and_b32_e32 v13, 0x1fff8, v60
	v_and_b32_e32 v15, 0x1fff8, v61
	ds_read_b64 v[100:101], v9
	ds_read_b64 v[102:103], v11
	ds_read_b64 v[104:105], v13
	ds_read_b64 v[112:113], v15
	v_and_b32_e32 v9, 0x1fff8, v62
	v_and_b32_e32 v11, 0x1fff8, v63
	v_and_b32_e32 v13, 0x1fff8, v54
	v_and_b32_e32 v15, 0x1fff8, v55
	ds_read_b64 v[114:115], v9
	ds_read_b64 v[118:119], v11
	ds_read_b64 v[120:121], v13
	ds_read_b64 v[122:123], v15
	s_setprio 1
	s_waitcnt lgkmcnt(7)
	v_cvt_pk_f32_fp8_e32 v[124:125], v100
	v_cvt_pk_f32_fp8_sdwa v[126:127], v100 src0_sel:WORD_1
	v_cvt_pk_f32_fp8_e32 v[128:129], v101
	v_cvt_pk_f32_fp8_sdwa v[100:101], v101 src0_sel:WORD_1
	s_waitcnt lgkmcnt(6)
	v_cvt_pk_f32_fp8_sdwa v[134:135], v103 src0_sel:WORD_1
	v_cvt_pk_f32_fp8_e32 v[130:131], v102
	s_waitcnt lgkmcnt(5)
	v_cvt_pk_f32_fp8_e32 v[138:139], v104
	v_cvt_pk_f32_fp8_sdwa v[140:141], v104 src0_sel:WORD_1
	v_cvt_pk_f32_fp8_e32 v[142:143], v105
	v_cvt_pk_f32_fp8_sdwa v[104:105], v105 src0_sel:WORD_1
	s_waitcnt lgkmcnt(4)
	v_cvt_pk_f32_fp8_sdwa v[148:149], v113 src0_sel:WORD_1
	v_pk_fma_f32 v[106:107], v[200:201], v[76:77], v[106:107] op_sel_hi:[1,0,1]
	s_waitcnt lgkmcnt(3)
	v_cvt_pk_f32_fp8_e32 v[152:153], v114
	v_cvt_pk_f32_fp8_sdwa v[154:155], v114 src0_sel:WORD_1
	v_cvt_pk_f32_fp8_e32 v[156:157], v115
	v_cvt_pk_f32_fp8_sdwa v[114:115], v115 src0_sel:WORD_1
	s_waitcnt lgkmcnt(2)
	v_cvt_pk_f32_fp8_sdwa v[162:163], v119 src0_sel:WORD_1
	v_pk_fma_f32 v[82:83], v[82:83], v[56:57], v[106:107] op_sel_hi:[1,0,1]
	v_mov_b32_e32 v106, v57
	v_cvt_pk_f32_fp8_e32 v[144:145], v112
	v_cvt_pk_f32_fp8_e32 v[158:159], v118
	v_cvt_pk_f32_fp8_sdwa v[160:161], v118 src0_sel:WORD_1
	v_cvt_pk_f32_fp8_e32 v[164:165], v119
	s_waitcnt lgkmcnt(1)
; #define GAS __attribute__((address_space(1)))
; __device__ __forceinline__ unsigned f2bf(float f) { unsigned u = __builtin_bit_cast(unsigned, f); return (u + 0x7fffu + ((u >> 16) & 1u)) >> 16; }
; template <int VVAR> __device__ __forceinline__ void peer_v_phase(LAS unsigned char* lds, int wave, int vcu, const unsigned char* __restrict__ VS_l, const unsigned* __restrict__ PW, bf16* __restrict__ Y) {
;     ...
; #pragma unroll 1
;     for (int it = 0; it < (VVAR == 5 ? 2 : 64); it += 2) {
;         V_HALF(pa, pb, it + 1);
;         V_HALF(pb, pa, it + 2);
;         if ((it & 3) == 2) {
;             const int blk = th * 128 + wave + 8 * (it >> 2);
;             bf16* yp = Y + ((size_t)blk * 1024 + cs * 8) * 64 + lane;
; #pragma unroll
;             for (int c = 0; c < 8; ++c) ((GAS unsigned short*)yp)[c * 64] = (unsigned short)f2bf(acc[c]);
; #pragma unroll
;             for (int c = 0; c < 8; ++c) acc[c] = 0.f;
	v_cvt_pk_f32_fp8_e32 v[118:119], v120
	v_cvt_pk_f32_fp8_sdwa v[168:169], v120 src0_sel:WORD_1
	v_cvt_pk_f32_fp8_e32 v[170:171], v121
	v_cvt_pk_f32_fp8_sdwa v[120:121], v121 src0_sel:WORD_1
	s_waitcnt lgkmcnt(0)
	v_cvt_pk_f32_fp8_sdwa v[176:177], v123 src0_sel:WORD_1
	v_pk_fma_f32 v[82:83], v[90:91], v[106:107], v[82:83] op_sel_hi:[1,0,1]
	v_pk_fma_f32 v[78:79], v[100:101], v[58:59], v[78:79] op_sel_hi:[1,0,1]
	v_pk_fma_f32 v[78:79], v[134:135], v[58:59], v[78:79] op_sel:[0,1,0] op_sel_hi:[1,1,1]
	v_pk_fma_f32 v[82:83], v[124:125], v[58:59], v[82:83] op_sel_hi:[1,0,1]
	v_mov_b32_e32 v90, v59
	v_pk_fma_f32 v[78:79], v[104:105], v[60:61], v[78:79] op_sel_hi:[1,0,1]
	v_pk_fma_f32 v[78:79], v[148:149], v[60:61], v[78:79] op_sel:[0,1,0] op_sel_hi:[1,1,1]
	v_pk_fma_f32 v[82:83], v[130:131], v[90:91], v[82:83] op_sel_hi:[1,0,1]
	v_pk_fma_f32 v[78:79], v[114:115], v[62:63], v[78:79] op_sel_hi:[1,0,1]
	v_pk_fma_f32 v[78:79], v[162:163], v[62:63], v[78:79] op_sel:[0,1,0] op_sel_hi:[1,1,1]
	v_pk_fma_f32 v[82:83], v[138:139], v[60:61], v[82:83] op_sel_hi:[1,0,1]
	v_mov_b32_e32 v116, v61
	v_cvt_pk_f32_fp8_e32 v[172:173], v122
	v_pk_fma_f32 v[78:79], v[120:121], v[54:55], v[78:79] op_sel_hi:[1,0,1]
	v_pk_fma_f32 v[82:83], v[144:145], v[116:117], v[82:83] op_sel_hi:[1,0,1]
	v_pk_fma_f32 v[78:79], v[176:177], v[54:55], v[78:79] op_sel:[0,1,0] op_sel_hi:[1,1,1]
	v_pk_fma_f32 v[82:83], v[152:153], v[62:63], v[82:83] op_sel_hi:[1,0,1]
	v_mov_b32_e32 v120, v63
	v_pk_fma_f32 v[82:83], v[158:159], v[120:121], v[82:83] op_sel_hi:[1,0,1]
	v_mov_b32_e32 v124, v55
	v_pk_fma_f32 v[82:83], v[118:119], v[54:55], v[82:83] op_sel_hi:[1,0,1]
	v_cvt_pk_f32_fp8_sdwa v[132:133], v102 src0_sel:WORD_1
	v_cvt_pk_f32_fp8_e32 v[102:103], v103
	v_pk_fma_f32 v[118:119], v[172:173], v[124:125], v[82:83] op_sel_hi:[1,0,1]
	v_pk_fma_f32 v[82:83], v[202:203], v[76:77], v[108:109] op_sel_hi:[1,0,1]
	v_pk_fma_f32 v[76:77], v[204:205], v[76:77], v[110:111] op_sel_hi:[1,0,1]
	v_pk_fma_f32 v[82:83], v[84:85], v[56:57], v[82:83] op_sel_hi:[1,0,1]
	v_pk_fma_f32 v[56:57], v[86:87], v[56:57], v[76:77] op_sel_hi:[1,0,1]
	v_cvt_pk_f32_fp8_sdwa v[146:147], v112 src0_sel:WORD_1
	v_cvt_pk_f32_fp8_e32 v[112:113], v113
	v_pk_fma_f32 v[56:57], v[96:97], v[106:107], v[56:57] op_sel_hi:[1,0,1]
	v_pk_fma_f32 v[82:83], v[92:93], v[106:107], v[82:83] op_sel_hi:[1,0,1]
	v_pk_fma_f32 v[56:57], v[128:129], v[58:59], v[56:57] op_sel_hi:[1,0,1]
	v_pk_fma_f32 v[82:83], v[126:127], v[58:59], v[82:83] op_sel_hi:[1,0,1]
	v_pk_fma_f32 v[56:57], v[102:103], v[90:91], v[56:57] op_sel_hi:[1,0,1]
	v_cvt_pk_f32_fp8_e32 v[178:179], v123
	v_pk_fma_f32 v[56:57], v[142:143], v[60:61], v[56:57] op_sel_hi:[1,0,1]
	v_pk_fma_f32 v[82:83], v[132:133], v[90:91], v[82:83] op_sel_hi:[1,0,1]
	v_pk_fma_f32 v[56:57], v[112:113], v[116:117], v[56:57] op_sel_hi:[1,0,1]
	v_pk_fma_f32 v[82:83], v[140:141], v[60:61], v[82:83] op_sel_hi:[1,0,1]
	v_pk_fma_f32 v[56:57], v[156:157], v[62:63], v[56:57] op_sel_hi:[1,0,1]
	v_pk_fma_f32 v[82:83], v[146:147], v[116:117], v[82:83] op_sel_hi:[1,0,1]
	v_pk_fma_f32 v[56:57], v[164:165], v[120:121], v[56:57] op_sel_hi:[1,0,1]
	v_pk_fma_f32 v[82:83], v[154:155], v[62:63], v[82:83] op_sel_hi:[1,0,1]
	v_pk_fma_f32 v[56:57], v[170:171], v[54:55], v[56:57] op_sel_hi:[1,0,1]
	v_pk_fma_f32 v[82:83], v[160:161], v[120:121], v[82:83] op_sel_hi:[1,0,1]
	v_pk_fma_f32 v[120:121], v[178:179], v[124:125], v[56:57] op_sel_hi:[1,0,1]
	v_cvt_pk_f32_fp8_sdwa v[174:175], v122 src0_sel:WORD_1
	v_pk_fma_f32 v[82:83], v[168:169], v[54:55], v[82:83] op_sel_hi:[1,0,1]
	v_pk_fma_f32 v[122:123], v[174:175], v[124:125], v[82:83] op_sel_hi:[1,0,1]
	v_mov_b32_e32 v124, v78
	v_mov_b32_e32 v125, v79
	s_setprio 0
	s_bitcmp0_b32 s17, 1
	s_cbranch_scc1 .LBB0_955
	s_lshl_b64 s[8:9], s[8:9], 17
	v_lshl_add_u64 v[54:55], v[0:1], 0, s[8:9]
	v_cvt_pk_bf16_f32 v9, v118, v119
	v_cvt_pk_bf16_f32 v11, v122, v123
	v_cvt_pk_bf16_f32 v13, v120, v121
	v_cvt_pk_bf16_f32 v15, v124, v125
	global_store_short v[54:55], v9, off
	global_store_short_d16_hi v[54:55], v9, off offset:128
	global_store_short v[54:55], v11, off offset:256
	global_store_short_d16_hi v[54:55], v11, off offset:384
	global_store_short v[54:55], v13, off offset:512
	global_store_short_d16_hi v[54:55], v13, off offset:640
	global_store_short v[54:55], v15, off offset:768
	global_store_short_d16_hi v[54:55], v15, off offset:896
	v_mov_b64_e32 v[118:119], 0
	v_mov_b64_e32 v[122:123], 0
	v_mov_b64_e32 v[120:121], 0
	v_mov_b64_e32 v[124:125], 0
	s_branch .LBB0_955
